# previous + latent-up-projection phase converts 7 instead of 3 expert-weight tiles per workgroup 128..255 (fills their idle time)
# speedup vs baseline: 1.0083x; 1.0016x over previous
; #define CQ_PULL(dst) do { __syncthreads(); if (tid == 0) qs[0] = CQ_CAN ? atomicAdd(ctr, 1) : NMT; __syncthreads(); dst = qs[0]; ++pulled; } while (0)
; #define CQ_LOAD(buf, slab, src, ldw) do { _Pragma("unroll") for (int r_ = 0; r_ < 4; ++r_) a[buf][r_] = __builtin_nontemporal_load((const f32x4*)(src + (size_t)((slab) * 32 + r_) * ldw)); } while (0)
; __device__ __forceinline__ void conv_queue(const P& p, LAS unsigned char* lds, int* ctr, int max_tiles) {
;     ...
;     int t_cur, t_nxt;
;     CQ_PULL(t_cur); if (t_cur >= NMT) { __syncthreads(); return; }
;     CQ_PULL(t_nxt);
;     f32x4 a[4][4];
;     ...
;     { CQ_SRC(t_cur, s0, l0); CQ_LOAD(0, 0, s0, l0); CQ_LOAD(1, 1, s0, l0); CQ_LOAD(2, 2, s0, l0); CQ_LOAD(3, 3, s0, l0); }
;     for (int it = 0;; ++it) {
;         const bool more = t_nxt < NMT, cur_w1 = t_cur < NM1;
;         if (tid == 0) qs[1 + (it & 1)] = (more && CQ_CAN) ? atomicAdd(ctr, 1) : NMT;
;         ++pulled;
;         CQ_PUT(0, 0); CQ_PUT(1, 1);
;         CQ_SRC(t_nxt < NMT ? t_nxt : 0, s1, l1);
;         if (more) { CQ_LOAD(0, 0, s1, l1); CQ_LOAD(1, 1, s1, l1); }
; __global__ void __launch_bounds__(512, 2) mega(P p, int lo, int hi, int bar_idx) {
;     ...
;         if (MOE_FP8 && G == 256 && bid >= 128) at::conv_queue(p, lds, (int*)(p.ws + WS_CTL + 61440) + 128, 3);
.LBB0_595:
	global_load_dwordx4 v[52:55], v[76:77], off nt
	global_load_dwordx4 v[56:59], v[78:79], off nt
	global_load_dwordx4 v[60:63], v[82:83], off nt
	global_load_dwordx4 v[64:67], v[80:81], off nt
	global_load_dwordx4 v[2:5], v[84:85], off nt
	global_load_dwordx4 v[6:9], v[88:89], off nt
	global_load_dwordx4 v[10:13], v[86:87], off nt
	global_load_dwordx4 v[14:17], v[90:91], off nt
	v_mov_b32_e32 v18, s11
	ds_read_b32 v18, v18
	s_waitcnt lgkmcnt(0)
	v_readfirstlane_b32 s28, v18
	s_cmpk_lt_i32 s28, 0x3000
	s_cselect_b64 s[14:15], -1, 0
	s_mov_b64 s[4:5], exec
	v_readlane_b32 s6, v242, 31
	v_readlane_b32 s7, v242, 32
	s_and_b64 s[6:7], s[4:5], s[6:7]
	s_mov_b64 exec, s[6:7]
	s_cbranch_execz .LBB0_601
	s_cmp_lt_u32 s2, 7
	s_cselect_b64 s[6:7], -1, 0
	s_and_b64 s[6:7], s[14:15], s[6:7]
	s_andn2_b64 vcc, exec, s[6:7]
	v_mov_b32_e32 v18, 0x3000
	s_cbranch_vccnz .LBB0_600
	s_mov_b64 s[10:11], exec
	v_mbcnt_lo_u32_b32 v18, s10, 0
	v_mbcnt_hi_u32_b32 v18, s11, v18
	v_cmp_eq_u32_e32 vcc, 0, v18
	s_and_saveexec_b64 s[6:7], vcc
	s_cbranch_execz .LBB0_599
	s_bcnt1_i32_b64 s8, s[10:11]
	v_mov_b32_e32 v73, s8
	global_atomic_add v73, v19, v73, s[0:1] sc0
